# expert-GEMM unit headers (P7, P8): the dependent LDS table reads issued together with counted waits
# speedup vs baseline: 1.0069x; 1.0009x over previous
.LBB0_908:
	s_add_i32 s59, s31, 1
	s_lshl_b32 s6, s30, 2
	s_add_i32 s30, s6, 0
	s_add_i32 s6, s30, 0x25000
	v_mov_b32_e32 v242, s6
	ds_read_b32 v242, v242
	s_cmp_ge_u32 s59, s23
	s_cbranch_scc1 .LBB0_911
	s_lshl_b32 s6, s59, 4
	s_add_i32 s7, s6, 0
	s_add_i32 s6, s7, 0x25200
	v_mov_b32_e32 v2, s6
	ds_read_b32 v2, v2
	s_add_i32 s7, s7, 0x25204
	v_mov_b32_e32 v243, s7
	ds_read2_b32 v[244:245], v243 offset1:1
	s_lshl_b32 s25, s59, 10
	s_add_i32 s25, s25, 0x20000
	v_lshl_add_u32 v246, v224, 2, s25
	v_lshl_add_u32 v247, v226, 2, s25
	ds_read2st64_b32 v[248:249], v246 offset1:2
	ds_read2st64_b32 v[250:251], v247 offset1:2
	s_waitcnt lgkmcnt(3)
	v_readfirstlane_b32 s6, v2
	s_cmp_lt_i32 s6, 0
	s_cbranch_scc1 .LBB0_911
	s_mov_b64 s[36:37], -1
	s_mov_b32 s24, s6
	s_mov_b32 s57, s59
	s_waitcnt lgkmcnt(2)
	v_readfirstlane_b32 s58, v244
	v_readfirstlane_b32 s26, v245
	s_branch .LBB0_912

.LBB0_912:
	s_lshl_b32 s10, s60, 8
	v_cndmask_b32_e64 v3, 0, 1, s[36:37]
	v_cmp_ne_u32_e64 s[6:7], 1, v3
	s_mov_b64 s[28:29], s[8:9]
	s_waitcnt lgkmcnt(0)
	v_subrev_u32_e32 v2, s10, v242
	v_cmp_gt_i32_e32 vcc, s53, v2
	s_nop 1
	v_cndmask_b32_e64 v2, 0, 1, vcc
	s_nop 0
	v_readfirstlane_b32 s10, v2
	s_bitcmp1_b32 s10, 0
	s_cselect_b64 s[10:11], -1, 0
	s_andn2_b64 vcc, exec, s[36:37]
	s_cbranch_vccnz .LBB0_914
	s_ashr_i32 s25, s24, 31
	s_ashr_i32 s27, s26, 31
	s_lshl_b64 s[28:29], s[24:25], 23
	s_lshl_b64 s[38:39], s[26:27], 19
	s_add_u32 s25, s3, s28
	s_addc_u32 s27, s21, s29
	s_add_u32 s28, s25, s38
	s_addc_u32 s29, s27, s39
.LBB0_914:
	s_and_b64 vcc, exec, s[6:7]
	v_mov_b32_e32 v236, v214
	v_mov_b32_e32 v237, v212
	v_mov_b32_e32 v238, v210
	v_mov_b32_e32 v239, v208
	s_cbranch_vccnz .LBB0_916
	v_lshl_add_u32 v236, v248, 11, v225
	v_lshl_add_u32 v237, v250, 11, v227
	v_lshl_add_u32 v238, v249, 11, v225
	v_lshl_add_u32 v239, v251, 11, v227

.LBB0_945:
	s_add_i32 s57, s59, 1
	s_add_i32 s7, s57, s23
	s_lshl_b32 s6, s6, 2
	s_add_i32 s60, s6, 0
	s_add_i32 s6, s60, 0x25000
	v_mov_b32_e32 v242, s6
	ds_read_b32 v242, v242
	s_cmp_gt_u32 s7, 19
	s_cbranch_scc1 .LBB0_948
	s_lshl_b32 s10, s7, 4
	s_add_i32 s11, s10, 0
	s_add_i32 s10, s11, 0x25200
	v_mov_b32_e32 v2, s10
	ds_read_b32 v2, v2
	s_add_i32 s11, s11, 0x25204
	v_mov_b32_e32 v243, s11
	ds_read2_b32 v[244:245], v243 offset1:1
	s_lshl_b32 s25, s7, 10
	s_add_i32 s25, s25, 0x20000
	v_lshl_add_u32 v246, v224, 2, s25
	v_lshl_add_u32 v247, v225, 2, s25
	ds_read2st64_b32 v[248:249], v246 offset1:2
	ds_read2st64_b32 v[250:251], v247 offset1:2
	s_waitcnt lgkmcnt(3)
	v_readfirstlane_b32 s10, v2
	s_cmp_lt_i32 s10, 0
	s_cbranch_scc1 .LBB0_948
	s_mov_b64 s[34:35], -1
	s_mov_b32 s24, s10
	s_mov_b32 s55, s7
	s_waitcnt lgkmcnt(2)
	v_readfirstlane_b32 s56, v244
	v_readfirstlane_b32 s26, v245
	s_branch .LBB0_949

.LBB0_949:
	s_lshl_b32 s10, s58, 8
	v_cndmask_b32_e64 v3, 0, 1, s[34:35]
	v_cmp_ne_u32_e64 s[6:7], 1, v3
	s_mov_b64 s[28:29], s[8:9]
	s_waitcnt lgkmcnt(0)
	v_subrev_u32_e32 v2, s10, v242
	v_cmp_gt_i32_e32 vcc, s51, v2
	s_nop 1
	v_cndmask_b32_e64 v2, 0, 1, vcc
	s_nop 0
	v_readfirstlane_b32 s10, v2
	s_bitcmp1_b32 s10, 0
	s_cselect_b64 s[10:11], -1, 0
	s_andn2_b64 vcc, exec, s[34:35]
	s_cbranch_vccnz .LBB0_951
	s_ashr_i32 s25, s24, 31
	s_ashr_i32 s27, s26, 31
	s_lshl_b64 s[28:29], s[24:25], 23
	s_lshl_b64 s[36:37], s[26:27], 19
	s_add_u32 s25, s3, s28
	s_addc_u32 s27, s21, s29
	s_add_u32 s28, s25, s36
	s_addc_u32 s29, s27, s37
.LBB0_951:
	s_and_b64 vcc, exec, s[6:7]
	v_mov_b32_e32 v236, v214
	v_mov_b32_e32 v237, v212
	v_mov_b32_e32 v238, v210
	v_mov_b32_e32 v239, v208
	s_cbranch_vccnz .LBB0_953
	v_lshl_add_u32 v236, v248, 11, v227
	v_lshl_add_u32 v237, v250, 11, v226
	v_lshl_add_u32 v238, v249, 11, v227
	v_lshl_add_u32 v239, v251, 11, v226

.LBB0_1110:
	s_add_i32 s57, s59, 1
	s_lshl_b32 s6, s6, 2
	s_add_i32 s62, s6, 0
	s_add_i32 s61, s62, 0x25000
	v_mov_b32_e32 v246, s61
	ds_read_b32 v246, v246
	s_cmp_gt_u32 s59, 18
	s_cbranch_scc1 .LBB0_1113
	s_lshl_b32 s7, s57, 4
	s_add_i32 s19, s7, 0
	s_add_i32 s7, s19, 0x25200
	v_mov_b32_e32 v2, s7
	ds_read_b32 v2, v2
	s_add_i32 s18, s19, 0x25204
	v_mov_b32_e32 v247, s18
	ds_read2_b32 v[248:249], v247 offset1:1
	s_waitcnt lgkmcnt(1)
	v_readfirstlane_b32 s7, v2
	s_cmp_lt_i32 s7, 0
	s_cbranch_scc1 .LBB0_1113
	s_mov_b64 s[30:31], -1
	s_mov_b32 s20, s7
	s_lshl_b32 s19, s20, 2
	s_add_i32 s19, s19, 0x25100
	v_mov_b32_e32 v250, s19
	ds_read_b32 v250, v250
	s_waitcnt lgkmcnt(1)
	v_readfirstlane_b32 s56, v248
	v_readfirstlane_b32 s18, v249
	s_branch .LBB0_1114

.LBB0_1114:
	s_lshl_b32 s60, s58, 8
	v_cndmask_b32_e64 v3, 0, 1, s[30:31]
	v_cmp_ne_u32_e64 s[6:7], 1, v3
	s_mov_b64 s[22:23], s[28:29]
	s_waitcnt lgkmcnt(0)
	v_subrev_u32_e32 v2, s60, v246
	v_cmp_gt_i32_e32 vcc, s53, v2
	s_nop 1
	v_cndmask_b32_e64 v2, 0, 1, vcc
	s_nop 0
	v_readfirstlane_b32 s19, v2
	s_bitcmp1_b32 s19, 0
	s_cselect_b64 s[34:35], -1, 0
	s_andn2_b64 vcc, exec, s[30:31]
	s_cbranch_vccnz .LBB0_1116
	v_readfirstlane_b32 s19, v250
	s_add_i32 s22, s19, s56
	s_ashr_i32 s23, s22, 31
	s_lshl_b64 s[22:23], s[22:23], 19
	s_add_u32 s22, s42, s22
	s_addc_u32 s23, s43, s23
